# baseline (speedup 1.0000x reference)
.LBB1_2:
	s_add_i32 s25, s26, 2
	v_add_u32_e32 v208, s14, v207
	ds_read_b64_tr_b16 v[178:179], v208 offset:24576
	ds_read_b64_tr_b16 v[180:181], v208 offset:25088
	v_mfma_f32_32x32x16_f16 v[98:113], v[174:177], v[138:141], v[34:49]
	v_add_f32_e32 v82, v66, v67
	v_add_f32_e32 v82, v68, v82
	v_add_f32_e32 v82, v69, v82
	v_add_f32_e32 v82, v70, v82
	v_add_f32_e32 v82, v71, v82
	v_cvt_pk_f16_f32 v142, v66, v67
	v_cvt_pk_f16_f32 v143, v68, v69
	ds_read_b64_tr_b16 v[174:175], v208 offset:28672
	ds_read_b64_tr_b16 v[176:177], v208 offset:29184
	v_add_f32_e32 v66, v72, v82
	v_mfma_f32_32x32x16_f16 v[82:97], v[170:173], v[138:141], v[34:49]
	v_add_f32_e32 v66, v73, v66
	v_add_f32_e32 v66, v74, v66
	v_add_f32_e32 v66, v75, v66
	v_cvt_pk_f16_f32 v144, v70, v71
	v_cvt_pk_f16_f32 v145, v72, v73
	ds_read_b64_tr_b16 v[170:171], v208 offset:25600
	ds_read_b64_tr_b16 v[172:173], v208 offset:26112
	v_mfma_f32_32x32x16_f16 v[98:113], v[166:169], v[130:133], v[98:113]
	v_add_f32_e32 v66, v76, v66
	v_add_f32_e32 v66, v77, v66
	v_add_f32_e32 v66, v78, v66
	v_add_f32_e32 v66, v79, v66
	v_cvt_pk_f16_f32 v134, v74, v75
	v_cvt_pk_f16_f32 v135, v76, v77
	ds_read_b64_tr_b16 v[74:75], v208 offset:29696
	ds_read_b64_tr_b16 v[76:77], v208 offset:30208
	v_mfma_f32_32x32x16_f16 v[82:97], v[162:165], v[130:133], v[82:97]
	v_add_f32_e32 v66, v80, v66
	v_add_f32_e32 v66, v81, v66
	v_add_f32_e32 v66, v50, v66
	v_add_f32_e32 v66, v51, v66
	v_cvt_pk_f16_f32 v136, v78, v79
	v_cvt_pk_f16_f32 v137, v80, v81
	ds_read_b64_tr_b16 v[70:71], v208 offset:26624
	ds_read_b64_tr_b16 v[72:73], v208 offset:27136
	v_mfma_f32_32x32x16_f16 v[98:113], v[158:161], v[126:129], v[98:113]
	v_add_f32_e32 v66, v52, v66
	v_add_f32_e32 v66, v53, v66
	v_add_f32_e32 v66, v54, v66
	v_add_f32_e32 v78, v55, v66
	v_cvt_pk_f16_f32 v122, v50, v51
	v_cvt_pk_f16_f32 v123, v52, v53
	ds_read_b64_tr_b16 v[66:67], v208 offset:30720
	ds_read_b64_tr_b16 v[68:69], v208 offset:31232
	v_mfma_f32_32x32x16_f16 v[82:97], v[154:157], v[126:129], v[82:97]
	v_add_f32_e32 v50, v56, v78
	v_add_f32_e32 v50, v57, v50
	v_add_f32_e32 v50, v58, v50
	v_add_f32_e32 v50, v59, v50
	v_cvt_pk_f16_f32 v124, v54, v55
	v_cvt_pk_f16_f32 v125, v56, v57
	ds_read_b64_tr_b16 v[54:55], v208 offset:27648
	ds_read_b64_tr_b16 v[56:57], v208 offset:28160
	v_mfma_f32_32x32x16_f16 v[98:113], v[150:153], v[118:121], v[98:113]
	v_add_f32_e32 v50, v60, v50
	v_add_f32_e32 v50, v61, v50
	v_add_f32_e32 v50, v62, v50
	v_add_f32_e32 v78, v63, v50
	v_cvt_pk_f16_f32 v114, v58, v59
	v_cvt_pk_f16_f32 v115, v60, v61
	ds_read_b64_tr_b16 v[50:51], v208 offset:31744
	ds_read_b64_tr_b16 v[52:53], v208 offset:32256
	v_mfma_f32_32x32x16_f16 v[82:97], v[146:149], v[118:121], v[82:97]
	v_add_f32_e32 v58, v64, v78
	v_add_f32_e32 v78, v65, v58
	v_cvt_pk_f16_f32 v116, v62, v63
	v_cvt_pk_f16_f32 v117, v64, v65
	s_add_i32 s14, s27, s34
	s_mov_b32 m0, s14
	s_nop 0
	global_load_lds_dwordx4 v220, s[44:45]
	s_add_u32 s44, s44, 0x20000
	s_addc_u32 s45, s45, 0
	s_add_i32 s14, s23, s35
	s_mov_b32 m0, s14
	s_nop 0
	global_load_lds_dwordx4 v221, s[46:47]
	s_add_u32 s46, s46, 0x20000
	s_addc_u32 s47, s47, 0
	s_lshr_b32 s37, s33, s25
	s_bitcmp0_b32 s37, 0
	s_cbranch_scc0 .LBB1_12

.LBB1_6:
	s_add_i32 s14, s23, 0x2000
	s_cmpk_lg_i32 s23, 0x4000
	s_cselect_b32 s36, s14, 0
	v_add_u32_e32 v208, s27, v207
	ds_read_b64_tr_b16 v[154:155], v208 offset:24576
	ds_read_b64_tr_b16 v[156:157], v208 offset:25088
	v_mfma_f32_32x32x16_f16 v[66:81], v[58:61], v[138:141], v[34:49]
	v_add_f32_e32 v50, v98, v99
	v_add_f32_e32 v50, v100, v50
	v_add_f32_e32 v50, v101, v50
	v_add_f32_e32 v50, v102, v50
	v_add_f32_e32 v50, v103, v50
	v_cvt_pk_f16_f32 v142, v98, v99
	v_cvt_pk_f16_f32 v143, v100, v101
	ds_read_b64_tr_b16 v[150:151], v208 offset:28672
	ds_read_b64_tr_b16 v[152:153], v208 offset:29184
	v_add_f32_e32 v50, v104, v50
	v_add_f32_e32 v50, v105, v50
	v_add_f32_e32 v50, v106, v50
	v_add_f32_e32 v98, v107, v50
	v_mfma_f32_32x32x16_f16 v[50:65], v[146:149], v[138:141], v[34:49]
	v_cvt_pk_f16_f32 v144, v102, v103
	v_cvt_pk_f16_f32 v145, v104, v105
	ds_read_b64_tr_b16 v[146:147], v208 offset:25600
	ds_read_b64_tr_b16 v[148:149], v208 offset:26112
	v_mfma_f32_32x32x16_f16 v[66:81], v[178:181], v[130:133], v[66:81]
	v_add_f32_e32 v98, v108, v98
	v_add_f32_e32 v98, v109, v98
	v_add_f32_e32 v98, v110, v98
	v_add_f32_e32 v98, v111, v98
	v_cvt_pk_f16_f32 v134, v106, v107
	v_cvt_pk_f16_f32 v135, v108, v109
	ds_read_b64_tr_b16 v[106:107], v208 offset:29696
	ds_read_b64_tr_b16 v[108:109], v208 offset:30208
	v_mfma_f32_32x32x16_f16 v[50:65], v[170:173], v[130:133], v[50:65]
	v_add_f32_e32 v98, v112, v98
	v_add_f32_e32 v98, v113, v98
	v_add_f32_e32 v98, v82, v98
	v_add_f32_e32 v98, v83, v98
	v_cvt_pk_f16_f32 v136, v110, v111
	v_cvt_pk_f16_f32 v137, v112, v113
	ds_read_b64_tr_b16 v[102:103], v208 offset:26624
	ds_read_b64_tr_b16 v[104:105], v208 offset:27136
	v_mfma_f32_32x32x16_f16 v[66:81], v[174:177], v[126:129], v[66:81]
	v_add_f32_e32 v98, v84, v98
	v_add_f32_e32 v98, v85, v98
	v_add_f32_e32 v98, v86, v98
	v_add_f32_e32 v110, v87, v98
	v_cvt_pk_f16_f32 v122, v82, v83
	v_cvt_pk_f16_f32 v123, v84, v85
	ds_read_b64_tr_b16 v[98:99], v208 offset:30720
	ds_read_b64_tr_b16 v[100:101], v208 offset:31232
	v_mfma_f32_32x32x16_f16 v[50:65], v[162:165], v[126:129], v[50:65]
	v_add_f32_e32 v82, v88, v110
	v_add_f32_e32 v82, v89, v82
	v_add_f32_e32 v82, v90, v82
	v_add_f32_e32 v82, v91, v82
	v_cvt_pk_f16_f32 v124, v86, v87
	v_cvt_pk_f16_f32 v125, v88, v89
	ds_read_b64_tr_b16 v[86:87], v208 offset:27648
	ds_read_b64_tr_b16 v[88:89], v208 offset:28160
	v_mfma_f32_32x32x16_f16 v[66:81], v[166:169], v[118:121], v[66:81]
	v_add_f32_e32 v82, v92, v82
	v_add_f32_e32 v82, v93, v82
	v_add_f32_e32 v82, v94, v82
	v_add_f32_e32 v110, v95, v82
	v_cvt_pk_f16_f32 v114, v90, v91
	v_cvt_pk_f16_f32 v115, v92, v93
	ds_read_b64_tr_b16 v[82:83], v208 offset:31744
	ds_read_b64_tr_b16 v[84:85], v208 offset:32256
	v_mfma_f32_32x32x16_f16 v[50:65], v[158:161], v[118:121], v[50:65]
	v_add_f32_e32 v90, v96, v110
	v_add_f32_e32 v110, v97, v90
	v_cvt_pk_f16_f32 v116, v94, v95
	v_cvt_pk_f16_f32 v117, v96, v97
	s_add_i32 s14, s23, s34
	s_mov_b32 m0, s14
	s_nop 0
	global_load_lds_dwordx4 v220, s[44:45]
	s_add_u32 s44, s44, 0x20000
	s_addc_u32 s45, s45, 0
	s_add_i32 s14, s36, s35
	s_mov_b32 m0, s14
	s_nop 0
	global_load_lds_dwordx4 v221, s[46:47]
	s_add_u32 s46, s46, 0x20000
	s_addc_u32 s47, s47, 0
	s_bitcmp0_b32 s37, 1
	s_cbranch_scc0 .LBB1_16
